# speedup vs baseline: 1.0116x; 1.0116x over previous
.LBB4_18:
.LBB4_24:
	s_and_b64 s[50:51], s[42:43], exec
	s_cselect_b32 s52, s39, s47
	s_cselect_b32 s53, s38, s46
	s_cselect_b32 s54, s41, s45
	s_cselect_b32 s55, s40, s44
	s_add_u32 s28, s46, 0x100
	s_addc_u32 s84, s47, 0
	s_and_b64 s[50:51], s[48:49], exec
	s_cselect_b32 s51, s52, s84
	s_cselect_b32 s50, s53, s28
	s_add_u32 s28, s44, 0x100
	s_addc_u32 s84, s45, 0
	s_and_b64 s[48:49], s[48:49], exec
	s_cselect_b32 s49, s54, s84
	s_cselect_b32 s48, s55, s28
	s_mov_b32 m0, s59
	v_add_u32_e32 v229, s76, v234
	v_lshl_add_u64 v[130:131], s[48:49], 0, v[216:217]
	ds_read_b128 v[74:77], v229
	ds_read_b128 v[86:89], v229 offset:1024
	ds_read_b128 v[98:101], v229 offset:2048
	ds_read_b128 v[106:109], v229 offset:3072
	global_load_lds_dwordx4 v[130:131], off
	v_lshl_add_u64 v[132:133], s[48:49], 0, v[218:219]
	s_mov_b32 m0, s60
	s_nop 0
	global_load_lds_dwordx4 v[132:133], off
	s_barrier
	s_waitcnt lgkmcnt(0)
	s_setprio 1
	s_waitcnt lgkmcnt(0)
	v_mfma_f32_16x16x32_f16 v[94:97], v[74:77], v[46:49], 0
	v_mfma_f32_16x16x32_f16 v[46:49], v[98:101], v[46:49], 0
	v_mfma_f32_16x16x32_f16 v[94:97], v[86:89], v[50:53], v[94:97]
	v_mfma_f32_16x16x32_f16 v[50:53], v[106:109], v[50:53], v[46:49]
	v_mfma_f32_16x16x32_f16 v[46:49], v[74:77], v[38:41], 0
	v_mfma_f32_16x16x32_f16 v[38:41], v[98:101], v[38:41], 0
	v_mfma_f32_16x16x32_f16 v[110:113], v[106:109], v[42:45], v[38:41]
	v_mfma_f32_16x16x32_f16 v[38:41], v[74:77], v[30:33], 0
	v_mfma_f32_16x16x32_f16 v[30:33], v[98:101], v[30:33], 0
	v_mfma_f32_16x16x32_f16 v[174:177], v[106:109], v[34:37], v[30:33]
	v_mfma_f32_16x16x32_f16 v[30:33], v[74:77], v[22:25], 0
	v_mfma_f32_16x16x32_f16 v[22:25], v[98:101], v[22:25], 0
	v_mfma_f32_16x16x32_f16 v[102:105], v[86:89], v[42:45], v[46:49]
	v_mfma_f32_16x16x32_f16 v[170:173], v[86:89], v[34:37], v[38:41]
	v_mfma_f32_16x16x32_f16 v[178:181], v[86:89], v[26:29], v[30:33]
	v_mfma_f32_16x16x32_f16 v[182:185], v[106:109], v[26:29], v[22:25]
	s_setprio 0
	s_mov_b32 m0, s58
	s_barrier
	ds_read_b128 v[34:37], v237 offset:16384
	ds_read_b128 v[46:49], v237 offset:17408
	ds_read_b128 v[114:117], v237 offset:18432
	ds_read_b128 v[118:121], v237 offset:19456
	ds_read_b128 v[122:125], v237 offset:20480
	ds_read_b128 v[126:129], v237 offset:21504
	ds_read_b128 v[166:169], v237 offset:22528
	ds_read_b128 v[186:189], v237 offset:23552
	global_load_lds_dwordx4 v220, s[50:51]
	s_mov_b32 m0, s62
	s_nop 0
	global_load_lds_dwordx4 v226, s[50:51]
	s_barrier
	s_waitcnt lgkmcnt(0)
	s_setprio 1
	s_waitcnt lgkmcnt(0)
	v_mfma_f32_16x16x32_f16 v[22:25], v[6:9], v[34:37], 0
	v_mfma_f32_16x16x32_f16 v[30:33], v[6:9], v[114:117], 0
	v_mfma_f32_16x16x32_f16 v[42:45], v[6:9], v[122:125], 0
	v_mfma_f32_16x16x32_f16 v[6:9], v[6:9], v[166:169], 0
	v_mfma_f32_16x16x32_f16 v[22:25], v[10:13], v[46:49], v[22:25]
	v_mfma_f32_16x16x32_f16 v[26:29], v[14:17], v[34:37], 0
	v_mfma_f32_16x16x32_f16 v[30:33], v[10:13], v[118:121], v[30:33]
	v_mfma_f32_16x16x32_f16 v[38:41], v[14:17], v[114:117], 0
	v_mfma_f32_16x16x32_f16 v[42:45], v[10:13], v[126:129], v[42:45]
	v_mfma_f32_16x16x32_f16 v[134:137], v[14:17], v[122:125], 0
	v_mfma_f32_16x16x32_f16 v[6:9], v[10:13], v[186:189], v[6:9]
	v_mfma_f32_16x16x32_f16 v[10:13], v[14:17], v[166:169], 0
	v_mfma_f32_16x16x32_f16 v[26:29], v[18:21], v[46:49], v[26:29]
	v_mfma_f32_16x16x32_f16 v[38:41], v[18:21], v[118:121], v[38:41]
	v_mfma_f32_16x16x32_f16 v[134:137], v[18:21], v[126:129], v[134:137]
	v_mfma_f32_16x16x32_f16 v[14:17], v[18:21], v[186:189], v[10:13]
	s_setprio 0
	s_barrier
	s_add_u32 s86, s48, 0x40000
	s_addc_u32 s87, s49, 0
	s_add_i32 s84, s76, s57
	v_lshl_add_u64 v[10:11], s[86:87], 0, v[216:217]
	s_mov_b32 m0, s84
	s_add_i32 s85, s84, 0x2000
	global_load_lds_dwordx4 v[10:11], off
	v_lshl_add_u64 v[10:11], s[86:87], 0, v[218:219]
	s_mov_b32 m0, s85
	s_nop 0
	global_load_lds_dwordx4 v[10:11], off
	s_waitcnt vmcnt(6)
	s_cmp_gt_i32 s61, 44
	s_cbranch_scc1 .Lhka_done_a0
	s_cmp_lt_i32 s61, 1
	s_cbranch_scc1 .Lhka_ld_a0
	s_add_i32 s94, s75, s61
	s_mov_b32 s95, 0
	s_cmpk_gt_u32 s94, 0x15ff
	s_cselect_b32 s97, 0x7fffea00, 0
	s_cselect_b32 s96, 0x80, 0
	s_add_i32 s97, s97, s94
	s_lshl_b32 s94, s97, 1
	s_add_i32 s97, s94, 0x2c00
	s_mul_hi_u32 s98, s97, 0xba2e8ba3
	s_lshr_b32 s98, s98, 11
	s_mul_i32 s99, s98, 0x7ffff500
	s_add_i32 s99, s99, s97
	s_lshr_b32 s97, s99, 7
	s_mul_i32 s98, s98, 22
	s_add_i32 s97, s97, s98
	s_lshl_b32 s97, s97, 8
	s_and_b32 s94, s94, 0x7e
	s_or_b32 s96, s97, s96
	s_or_b32 s94, s96, s94
	s_lshl_b64 s[96:97], s[94:95], 11
	v_cvt_pk_f16_f32 v2, v2, v3
	v_cvt_pk_f16_f32 v3, v4, v5
	v_lshl_add_u64 v[4:5], v[224:225], 0, s[96:97]
	global_store_dwordx2 v[4:5], v[2:3], off
.Lhka_ld_a0:
	s_cmp_eq_u32 s61, 44
	s_cbranch_scc1 .Lhka_inc_a0
	s_add_i32 s94, s61, s33
	s_mov_b32 s95, 0
	s_cmpk_gt_u32 s94, 0x15ff
	s_cselect_b64 s[96:97], -1, 0
	s_and_b64 s[96:97], s[96:97], exec
	s_cselect_b32 s96, 0x7fffea00, 0
	s_cselect_b32 s98, s25, s15
	s_cselect_b32 s99, s24, s14
	s_add_i32 s96, s96, s94
	s_lshl_b32 s94, s96, 1
	s_addk_i32 s94, 0x2c00
	s_lshl_b64 s[96:97], s[94:95], 12
	s_add_u32 s96, s99, s96
	s_addc_u32 s97, s98, s97
	v_lshlrev_b32_e32 v4, 2, v214
	v_mov_b32_e32 v5, v221
	v_lshl_add_u64 v[4:5], s[96:97], 0, v[4:5]
	global_load_dwordx4 v[2:5], v[4:5], off nt

.Lhka_done_a0:
	s_barrier
	s_setprio 1
	v_mfma_f32_16x16x32_f16 v[10:13], v[74:77], v[34:37], 0
	v_mfma_f32_16x16x32_f16 v[138:141], v[86:89], v[46:49], v[10:13]
	v_mfma_f32_16x16x32_f16 v[10:13], v[98:101], v[34:37], 0
	v_mfma_f32_16x16x32_f16 v[142:145], v[106:109], v[46:49], v[10:13]
	v_mfma_f32_16x16x32_f16 v[10:13], v[74:77], v[114:117], 0
	v_mfma_f32_16x16x32_f16 v[146:149], v[86:89], v[118:121], v[10:13]
	v_mfma_f32_16x16x32_f16 v[10:13], v[98:101], v[114:117], 0
	v_mfma_f32_16x16x32_f16 v[150:153], v[106:109], v[118:121], v[10:13]
	v_mfma_f32_16x16x32_f16 v[10:13], v[74:77], v[122:125], 0
	v_mfma_f32_16x16x32_f16 v[154:157], v[86:89], v[126:129], v[10:13]
	v_mfma_f32_16x16x32_f16 v[10:13], v[98:101], v[122:125], 0
	v_mfma_f32_16x16x32_f16 v[158:161], v[106:109], v[126:129], v[10:13]
	v_mfma_f32_16x16x32_f16 v[10:13], v[74:77], v[166:169], 0
	v_mfma_f32_16x16x32_f16 v[162:165], v[86:89], v[186:189], v[10:13]
	v_mfma_f32_16x16x32_f16 v[10:13], v[98:101], v[166:169], 0
	v_mfma_f32_16x16x32_f16 v[166:169], v[106:109], v[186:189], v[10:13]
	s_setprio 0
	v_add_u32_e32 v231, 0x18000, v235
	s_barrier
	s_nop 3
	ds_read_b128 v[10:13], v231
	ds_read_b128 v[186:189], v231 offset:1024
	ds_read_b128 v[190:193], v231 offset:2048
	ds_read_b128 v[194:197], v231 offset:3072
	s_mov_b32 m0, s63
	ds_read_b128 v[122:125], v237 offset:32768
	ds_read_b128 v[126:129], v237 offset:33792
	ds_read_b128 v[118:121], v237 offset:34816
	ds_read_b128 v[210:213], v237 offset:35840
	ds_read_b128 v[202:205], v237 offset:36864
	ds_read_b128 v[206:209], v237 offset:37888
	ds_read_b128 v[18:21], v237 offset:38912
	ds_read_b128 v[198:201], v237 offset:39936
	global_load_lds_dwordx4 v228, s[50:51]
	s_mov_b32 m0, s64
	s_nop 0
	global_load_lds_dwordx4 v230, s[50:51]
	s_waitcnt lgkmcnt(8)
	s_barrier
	s_waitcnt lgkmcnt(0)
	s_setprio 1
	s_waitcnt lgkmcnt(0)
	v_mfma_f32_16x16x32_f16 v[34:37], v[10:13], v[122:125], v[54:57]
	v_mfma_f32_16x16x32_f16 v[114:117], v[186:189], v[126:129], v[34:37]
	v_mfma_f32_16x16x32_f16 v[34:37], v[190:193], v[122:125], v[58:61]
	v_mfma_f32_16x16x32_f16 v[106:109], v[194:197], v[126:129], v[34:37]
	v_mfma_f32_16x16x32_f16 v[34:37], v[10:13], v[118:121], v[62:65]
	v_mfma_f32_16x16x32_f16 v[98:101], v[186:189], v[210:213], v[34:37]
	v_mfma_f32_16x16x32_f16 v[34:37], v[190:193], v[118:121], v[66:69]
	v_mfma_f32_16x16x32_f16 v[86:89], v[194:197], v[210:213], v[34:37]
	v_mfma_f32_16x16x32_f16 v[34:37], v[10:13], v[202:205], v[70:73]
	v_mfma_f32_16x16x32_f16 v[74:77], v[186:189], v[206:209], v[34:37]
	v_mfma_f32_16x16x32_f16 v[34:37], v[190:193], v[202:205], v[78:81]
	v_mfma_f32_16x16x32_f16 v[62:65], v[194:197], v[206:209], v[34:37]
	v_mfma_f32_16x16x32_f16 v[34:37], v[10:13], v[18:21], v[82:85]
	v_mfma_f32_16x16x32_f16 v[46:49], v[186:189], v[198:201], v[34:37]
	v_mfma_f32_16x16x32_f16 v[34:37], v[190:193], v[18:21], v[90:93]
	v_mfma_f32_16x16x32_f16 v[34:37], v[194:197], v[198:201], v[34:37]
	s_setprio 0
	s_barrier
.LBB4_30:
	v_mov_b32_e32 v227, v221
	v_lshl_add_u64 v[54:55], s[50:51], 0, v[220:221]
	v_lshl_add_u64 v[56:57], s[50:51], 0, v[226:227]
	s_add_i32 s50, 0, 0x1c000
	s_mov_b32 m0, s67
	v_add_u32_e32 v238, s50, v234
	v_lshl_add_u64 v[58:59], v[130:131], 0, s[30:31]
	ds_read_b128 v[240:243], v238
	ds_read_b128 v[244:247], v238 offset:1024
	ds_read_b128 v[248:251], v238 offset:2048
	ds_read_b128 v[252:255], v238 offset:3072
	global_load_lds_dwordx4 v[58:59], off
	v_lshl_add_u64 v[58:59], v[132:133], 0, s[30:31]
	s_mov_b32 m0, s68
	s_nop 0
	global_load_lds_dwordx4 v[58:59], off
	s_barrier
	s_waitcnt lgkmcnt(0)
	s_setprio 1
	s_waitcnt lgkmcnt(0)
	v_mfma_f32_16x16x32_f16 v[58:61], v[240:243], v[122:125], v[94:97]
	v_mfma_f32_16x16x32_f16 v[50:53], v[248:251], v[122:125], v[50:53]
	v_mfma_f32_16x16x32_f16 v[130:133], v[244:247], v[126:129], v[58:61]
	v_mfma_f32_16x16x32_f16 v[126:129], v[252:255], v[126:129], v[50:53]
	v_mfma_f32_16x16x32_f16 v[50:53], v[240:243], v[118:121], v[102:105]
	v_mfma_f32_16x16x32_f16 v[122:125], v[244:247], v[210:213], v[50:53]
	v_mfma_f32_16x16x32_f16 v[50:53], v[248:251], v[118:121], v[110:113]
	v_mfma_f32_16x16x32_f16 v[118:121], v[252:255], v[210:213], v[50:53]
	v_mfma_f32_16x16x32_f16 v[50:53], v[240:243], v[202:205], v[170:173]
	v_mfma_f32_16x16x32_f16 v[110:113], v[244:247], v[206:209], v[50:53]
	v_mfma_f32_16x16x32_f16 v[50:53], v[248:251], v[202:205], v[174:177]
	v_mfma_f32_16x16x32_f16 v[102:105], v[252:255], v[206:209], v[50:53]
	v_mfma_f32_16x16x32_f16 v[50:53], v[240:243], v[18:21], v[178:181]
	v_mfma_f32_16x16x32_f16 v[18:21], v[248:251], v[18:21], v[182:185]
	v_mfma_f32_16x16x32_f16 v[94:97], v[244:247], v[198:201], v[50:53]
	v_mfma_f32_16x16x32_f16 v[82:85], v[252:255], v[198:201], v[18:21]
	s_setprio 0
	s_mov_b32 m0, s69
	s_nop 3
	v_lshl_add_u64 v[18:19], v[54:55], 0, s[30:31]
	s_barrier
	ds_read_b128 v[66:69], v237 offset:49152
	ds_read_b128 v[78:81], v237 offset:50176
	ds_read_b128 v[170:173], v237 offset:51200
	ds_read_b128 v[174:177], v237 offset:52224
	ds_read_b128 v[178:181], v237 offset:53248
	ds_read_b128 v[182:185], v237 offset:54272
	ds_read_b128 v[198:201], v237 offset:55296
	ds_read_b128 v[202:205], v237 offset:56320
	global_load_lds_dwordx4 v[18:19], off
	v_lshl_add_u64 v[18:19], v[56:57], 0, s[30:31]
	s_mov_b32 m0, s70
	s_nop 0
	global_load_lds_dwordx4 v[18:19], off
	s_barrier
	s_waitcnt lgkmcnt(0)
	s_setprio 1
	s_waitcnt lgkmcnt(0)
	v_mfma_f32_16x16x32_f16 v[18:21], v[10:13], v[66:69], v[22:25]
	v_mfma_f32_16x16x32_f16 v[70:73], v[186:189], v[78:81], v[18:21]
	v_mfma_f32_16x16x32_f16 v[18:21], v[190:193], v[66:69], v[26:29]
	v_mfma_f32_16x16x32_f16 v[58:61], v[194:197], v[78:81], v[18:21]
	v_mfma_f32_16x16x32_f16 v[18:21], v[10:13], v[170:173], v[30:33]
	v_mfma_f32_16x16x32_f16 v[50:53], v[186:189], v[174:177], v[18:21]
	v_mfma_f32_16x16x32_f16 v[18:21], v[190:193], v[170:173], v[38:41]
	v_mfma_f32_16x16x32_f16 v[38:41], v[194:197], v[174:177], v[18:21]
	v_mfma_f32_16x16x32_f16 v[18:21], v[10:13], v[178:181], v[42:45]
	v_mfma_f32_16x16x32_f16 v[6:9], v[10:13], v[198:201], v[6:9]
	v_mfma_f32_16x16x32_f16 v[26:29], v[186:189], v[182:185], v[18:21]
	v_mfma_f32_16x16x32_f16 v[18:21], v[190:193], v[178:181], v[134:137]
	v_mfma_f32_16x16x32_f16 v[10:13], v[186:189], v[202:205], v[6:9]
	v_mfma_f32_16x16x32_f16 v[6:9], v[190:193], v[198:201], v[14:17]
	v_mfma_f32_16x16x32_f16 v[18:21], v[194:197], v[182:185], v[18:21]
	v_mfma_f32_16x16x32_f16 v[6:9], v[194:197], v[202:205], v[6:9]
	s_setprio 0
	s_barrier
	s_add_u32 s48, s48, 0x40080
	s_addc_u32 s49, s49, 0
	s_add_i32 s50, s50, s57
	v_lshl_add_u64 v[14:15], s[48:49], 0, v[216:217]
	s_mov_b32 m0, s50
	s_add_i32 s51, s50, 0x2000
	global_load_lds_dwordx4 v[14:15], off
	v_lshl_add_u64 v[14:15], s[48:49], 0, v[218:219]
	s_mov_b32 m0, s51
	s_nop 0
	global_load_lds_dwordx4 v[14:15], off
	s_waitcnt vmcnt(6)
	s_cmp_gt_i32 s61, 44
	s_cbranch_scc1 .Lhka_done_a1
	s_cmp_lt_i32 s61, 1
	s_cbranch_scc1 .Lhka_ld_a1
	s_add_i32 s94, s75, s61
	s_mov_b32 s95, 0
	s_cmpk_gt_u32 s94, 0x15ff
	s_cselect_b32 s97, 0x7fffea00, 0
	s_cselect_b32 s96, 0x80, 0
	s_add_i32 s97, s97, s94
	s_lshl_b32 s94, s97, 1
	s_add_i32 s97, s94, 0x2c00
	s_mul_hi_u32 s98, s97, 0xba2e8ba3
	s_lshr_b32 s98, s98, 11
	s_mul_i32 s99, s98, 0x7ffff500
	s_add_i32 s99, s99, s97
	s_lshr_b32 s97, s99, 7
	s_mul_i32 s98, s98, 22
	s_add_i32 s97, s97, s98
	s_lshl_b32 s97, s97, 8
	s_and_b32 s94, s94, 0x7e
	s_or_b32 s96, s97, s96
	s_or_b32 s94, s96, s94
	s_lshl_b64 s[96:97], s[94:95], 11
	v_cvt_pk_f16_f32 v2, v2, v3
	v_cvt_pk_f16_f32 v3, v4, v5
	v_lshl_add_u64 v[4:5], v[224:225], 0, s[96:97]
	global_store_dwordx2 v[4:5], v[2:3], off

.Lhka_done_a1:
	s_barrier
	s_setprio 1
	v_mfma_f32_16x16x32_f16 v[14:17], v[240:243], v[66:69], v[138:141]
	v_mfma_f32_16x16x32_f16 v[90:93], v[244:247], v[78:81], v[14:17]
	v_mfma_f32_16x16x32_f16 v[14:17], v[248:251], v[66:69], v[142:145]
	v_mfma_f32_16x16x32_f16 v[78:81], v[252:255], v[78:81], v[14:17]
	v_mfma_f32_16x16x32_f16 v[14:17], v[240:243], v[170:173], v[146:149]
	v_mfma_f32_16x16x32_f16 v[66:69], v[244:247], v[174:177], v[14:17]
	v_mfma_f32_16x16x32_f16 v[14:17], v[248:251], v[170:173], v[150:153]
	v_mfma_f32_16x16x32_f16 v[54:57], v[252:255], v[174:177], v[14:17]
	v_mfma_f32_16x16x32_f16 v[14:17], v[240:243], v[178:181], v[154:157]
	v_mfma_f32_16x16x32_f16 v[42:45], v[244:247], v[182:185], v[14:17]
	v_mfma_f32_16x16x32_f16 v[14:17], v[248:251], v[178:181], v[158:161]
	v_mfma_f32_16x16x32_f16 v[30:33], v[252:255], v[182:185], v[14:17]
	v_mfma_f32_16x16x32_f16 v[14:17], v[240:243], v[198:201], v[162:165]
	v_mfma_f32_16x16x32_f16 v[22:25], v[244:247], v[202:205], v[14:17]
	v_mfma_f32_16x16x32_f16 v[14:17], v[248:251], v[198:201], v[166:169]
	v_mfma_f32_16x16x32_f16 v[14:17], v[252:255], v[202:205], v[14:17]
	s_setprio 0
	s_cmp_lt_u32 s83, 3
	s_barrier
	s_cbranch_scc1 .LBB4_49
	s_add_u32 s46, s46, 0x180
	s_addc_u32 s47, s47, 0
	s_add_u32 s86, s44, 0x200
	s_addc_u32 s87, s45, 0
	s_mov_b32 s88, 4

.LBB4_40:
	s_add_u32 s28, s46, 0x80
	s_addc_u32 s48, s47, 0
	s_and_b64 s[44:45], s[44:45], exec
	s_cselect_b32 s45, s54, s87
	s_cselect_b32 s44, s55, s86
	s_mov_b32 m0, s59
	v_lshl_add_u64 v[182:183], s[44:45], 0, v[216:217]
	ds_read_b128 v[186:189], v229
	ds_read_b128 v[190:193], v229 offset:1024
	ds_read_b128 v[194:197], v229 offset:2048
	ds_read_b128 v[198:201], v229 offset:3072
	global_load_lds_dwordx4 v[182:183], off
	v_lshl_add_u64 v[184:185], s[44:45], 0, v[218:219]
	s_mov_b32 m0, s60
	s_cselect_b32 s49, s52, s48
	global_load_lds_dwordx4 v[184:185], off
	s_barrier
	s_waitcnt lgkmcnt(0)
	s_cselect_b32 s48, s53, s28
	s_setprio 1
	s_waitcnt lgkmcnt(0)
	v_mfma_f32_16x16x32_f16 v[130:133], v[186:189], v[174:177], v[130:133]
	v_mfma_f32_16x16x32_f16 v[126:129], v[194:197], v[174:177], v[126:129]
	v_mfma_f32_16x16x32_f16 v[122:125], v[186:189], v[166:169], v[122:125]
	v_mfma_f32_16x16x32_f16 v[118:121], v[194:197], v[166:169], v[118:121]
	v_mfma_f32_16x16x32_f16 v[110:113], v[186:189], v[158:161], v[110:113]
	v_mfma_f32_16x16x32_f16 v[102:105], v[194:197], v[158:161], v[102:105]
	v_mfma_f32_16x16x32_f16 v[94:97], v[186:189], v[150:153], v[94:97]
	v_mfma_f32_16x16x32_f16 v[82:85], v[194:197], v[150:153], v[82:85]
	v_mfma_f32_16x16x32_f16 v[130:133], v[190:193], v[178:181], v[130:133]
	v_mfma_f32_16x16x32_f16 v[126:129], v[198:201], v[178:181], v[126:129]
	v_mfma_f32_16x16x32_f16 v[122:125], v[190:193], v[170:173], v[122:125]
	v_mfma_f32_16x16x32_f16 v[118:121], v[198:201], v[170:173], v[118:121]
	v_mfma_f32_16x16x32_f16 v[110:113], v[190:193], v[162:165], v[110:113]
	v_mfma_f32_16x16x32_f16 v[102:105], v[198:201], v[162:165], v[102:105]
	v_mfma_f32_16x16x32_f16 v[94:97], v[190:193], v[154:157], v[94:97]
	v_mfma_f32_16x16x32_f16 v[82:85], v[198:201], v[154:157], v[82:85]
	s_setprio 0
	s_mov_b32 m0, s58
	s_barrier
	ds_read_b128 v[150:153], v237 offset:16384
	ds_read_b128 v[154:157], v237 offset:17408
	ds_read_b128 v[158:161], v237 offset:18432
	ds_read_b128 v[162:165], v237 offset:19456
	ds_read_b128 v[166:169], v237 offset:20480
	ds_read_b128 v[170:173], v237 offset:21504
	ds_read_b128 v[174:177], v237 offset:22528
	ds_read_b128 v[178:181], v237 offset:23552
	global_load_lds_dwordx4 v220, s[48:49]
	s_mov_b32 m0, s62
	s_nop 0
	global_load_lds_dwordx4 v226, s[48:49]
	s_barrier
	s_waitcnt lgkmcnt(0)
	s_setprio 1
	s_waitcnt lgkmcnt(0)
	v_mfma_f32_16x16x32_f16 v[70:73], v[134:137], v[150:153], v[70:73]
	v_mfma_f32_16x16x32_f16 v[58:61], v[142:145], v[150:153], v[58:61]
	v_mfma_f32_16x16x32_f16 v[50:53], v[134:137], v[158:161], v[50:53]
	v_mfma_f32_16x16x32_f16 v[38:41], v[142:145], v[158:161], v[38:41]
	v_mfma_f32_16x16x32_f16 v[26:29], v[134:137], v[166:169], v[26:29]
	v_mfma_f32_16x16x32_f16 v[18:21], v[142:145], v[166:169], v[18:21]
	v_mfma_f32_16x16x32_f16 v[10:13], v[134:137], v[174:177], v[10:13]
	v_mfma_f32_16x16x32_f16 v[6:9], v[142:145], v[174:177], v[6:9]
	v_mfma_f32_16x16x32_f16 v[70:73], v[138:141], v[154:157], v[70:73]
	v_mfma_f32_16x16x32_f16 v[58:61], v[146:149], v[154:157], v[58:61]
	v_mfma_f32_16x16x32_f16 v[50:53], v[138:141], v[162:165], v[50:53]
	v_mfma_f32_16x16x32_f16 v[38:41], v[146:149], v[162:165], v[38:41]
	v_mfma_f32_16x16x32_f16 v[26:29], v[138:141], v[170:173], v[26:29]
	v_mfma_f32_16x16x32_f16 v[18:21], v[146:149], v[170:173], v[18:21]
	v_mfma_f32_16x16x32_f16 v[10:13], v[138:141], v[178:181], v[10:13]
	v_mfma_f32_16x16x32_f16 v[6:9], v[146:149], v[178:181], v[6:9]
	s_setprio 0
	s_barrier
	s_add_u32 s90, s44, 0x40000
	s_addc_u32 s91, s45, 0
	s_mov_b32 m0, s84
	v_lshl_add_u64 v[134:135], s[90:91], 0, v[216:217]
	global_load_lds_dwordx4 v[134:135], off
	v_lshl_add_u64 v[134:135], s[90:91], 0, v[218:219]
	s_mov_b32 m0, s85
	s_nop 0
	global_load_lds_dwordx4 v[134:135], off
	s_waitcnt vmcnt(6)
	s_cmp_gt_i32 s61, 44
	s_cbranch_scc1 .Lhka_done_a2
	s_cmp_lt_i32 s61, 1
	s_cbranch_scc1 .Lhka_ld_a2
	s_add_i32 s94, s75, s61
	s_mov_b32 s95, 0
	s_cmpk_gt_u32 s94, 0x15ff
	s_cselect_b32 s97, 0x7fffea00, 0
	s_cselect_b32 s96, 0x80, 0
	s_add_i32 s97, s97, s94
	s_lshl_b32 s94, s97, 1
	s_add_i32 s97, s94, 0x2c00
	s_mul_hi_u32 s98, s97, 0xba2e8ba3
	s_lshr_b32 s98, s98, 11
	s_mul_i32 s99, s98, 0x7ffff500
	s_add_i32 s99, s99, s97
	s_lshr_b32 s97, s99, 7
	s_mul_i32 s98, s98, 22
	s_add_i32 s97, s97, s98
	s_lshl_b32 s97, s97, 8
	s_and_b32 s94, s94, 0x7e
	s_or_b32 s96, s97, s96
	s_or_b32 s94, s96, s94
	s_lshl_b64 s[96:97], s[94:95], 11
	v_cvt_pk_f16_f32 v2, v2, v3
	v_cvt_pk_f16_f32 v3, v4, v5
	v_lshl_add_u64 v[4:5], v[224:225], 0, s[96:97]
	global_store_dwordx2 v[4:5], v[2:3], off

.Lhka_done_a2:
	s_barrier
	s_setprio 1
	v_mfma_f32_16x16x32_f16 v[90:93], v[186:189], v[150:153], v[90:93]
	v_mfma_f32_16x16x32_f16 v[78:81], v[194:197], v[150:153], v[78:81]
	v_mfma_f32_16x16x32_f16 v[66:69], v[186:189], v[158:161], v[66:69]
	v_mfma_f32_16x16x32_f16 v[54:57], v[194:197], v[158:161], v[54:57]
	v_mfma_f32_16x16x32_f16 v[42:45], v[186:189], v[166:169], v[42:45]
	v_mfma_f32_16x16x32_f16 v[30:33], v[194:197], v[166:169], v[30:33]
	v_mfma_f32_16x16x32_f16 v[22:25], v[186:189], v[174:177], v[22:25]
	v_mfma_f32_16x16x32_f16 v[14:17], v[194:197], v[174:177], v[14:17]
	v_mfma_f32_16x16x32_f16 v[90:93], v[190:193], v[154:157], v[90:93]
	v_mfma_f32_16x16x32_f16 v[78:81], v[198:201], v[154:157], v[78:81]
	v_mfma_f32_16x16x32_f16 v[66:69], v[190:193], v[162:165], v[66:69]
	v_mfma_f32_16x16x32_f16 v[54:57], v[198:201], v[162:165], v[54:57]
	v_mfma_f32_16x16x32_f16 v[42:45], v[190:193], v[170:173], v[42:45]
	v_mfma_f32_16x16x32_f16 v[30:33], v[198:201], v[170:173], v[30:33]
	v_mfma_f32_16x16x32_f16 v[22:25], v[190:193], v[178:181], v[22:25]
	v_mfma_f32_16x16x32_f16 v[14:17], v[198:201], v[178:181], v[14:17]
	s_setprio 0
	s_barrier
	ds_read_b128 v[134:137], v231
	ds_read_b128 v[138:141], v231 offset:1024
	ds_read_b128 v[142:145], v231 offset:2048
	ds_read_b128 v[146:149], v231 offset:3072
	s_mov_b32 m0, s63
	ds_read_b128 v[174:177], v237 offset:32768
	ds_read_b128 v[178:181], v237 offset:33792
	ds_read_b128 v[166:169], v237 offset:34816
	ds_read_b128 v[170:173], v237 offset:35840
	ds_read_b128 v[158:161], v237 offset:36864
	ds_read_b128 v[162:165], v237 offset:37888
	ds_read_b128 v[150:153], v237 offset:38912
	ds_read_b128 v[154:157], v237 offset:39936
	global_load_lds_dwordx4 v228, s[48:49]
	s_mov_b32 m0, s64
	s_nop 0
	global_load_lds_dwordx4 v230, s[48:49]
	s_waitcnt lgkmcnt(8)
	s_barrier
	s_waitcnt lgkmcnt(0)
	s_setprio 1
	s_waitcnt lgkmcnt(0)
	v_mfma_f32_16x16x32_f16 v[114:117], v[134:137], v[174:177], v[114:117]
	v_mfma_f32_16x16x32_f16 v[106:109], v[142:145], v[174:177], v[106:109]
	v_mfma_f32_16x16x32_f16 v[98:101], v[134:137], v[166:169], v[98:101]
	v_mfma_f32_16x16x32_f16 v[86:89], v[142:145], v[166:169], v[86:89]
	v_mfma_f32_16x16x32_f16 v[74:77], v[134:137], v[158:161], v[74:77]
	v_mfma_f32_16x16x32_f16 v[62:65], v[142:145], v[158:161], v[62:65]
	v_mfma_f32_16x16x32_f16 v[46:49], v[134:137], v[150:153], v[46:49]
	v_mfma_f32_16x16x32_f16 v[34:37], v[142:145], v[150:153], v[34:37]
	v_mfma_f32_16x16x32_f16 v[114:117], v[138:141], v[178:181], v[114:117]
	v_mfma_f32_16x16x32_f16 v[106:109], v[146:149], v[178:181], v[106:109]
	v_mfma_f32_16x16x32_f16 v[98:101], v[138:141], v[170:173], v[98:101]
	v_mfma_f32_16x16x32_f16 v[86:89], v[146:149], v[170:173], v[86:89]
	v_mfma_f32_16x16x32_f16 v[74:77], v[138:141], v[162:165], v[74:77]
	v_mfma_f32_16x16x32_f16 v[62:65], v[146:149], v[162:165], v[62:65]
	v_mfma_f32_16x16x32_f16 v[46:49], v[138:141], v[154:157], v[46:49]
	v_mfma_f32_16x16x32_f16 v[34:37], v[146:149], v[154:157], v[34:37]
	s_setprio 0
	s_barrier
.LBB4_46:
	s_mov_b32 m0, s67
	v_lshl_add_u64 v[182:183], v[182:183], 0, s[30:31]
	ds_read_b128 v[190:193], v238
	ds_read_b128 v[194:197], v238 offset:1024
	ds_read_b128 v[198:201], v238 offset:2048
	ds_read_b128 v[202:205], v238 offset:3072
	global_load_lds_dwordx4 v[182:183], off
	v_lshl_add_u64 v[182:183], v[184:185], 0, s[30:31]
	s_mov_b32 m0, s68
	v_mov_b32_e32 v227, v221
	global_load_lds_dwordx4 v[182:183], off
	s_barrier
	s_waitcnt lgkmcnt(0)
	v_lshl_add_u64 v[186:187], s[48:49], 0, v[220:221]
	v_lshl_add_u64 v[188:189], s[48:49], 0, v[226:227]
	s_setprio 1
	s_waitcnt lgkmcnt(0)
	v_mfma_f32_16x16x32_f16 v[130:133], v[190:193], v[174:177], v[130:133]
	v_mfma_f32_16x16x32_f16 v[126:129], v[198:201], v[174:177], v[126:129]
	v_mfma_f32_16x16x32_f16 v[122:125], v[190:193], v[166:169], v[122:125]
	v_mfma_f32_16x16x32_f16 v[118:121], v[198:201], v[166:169], v[118:121]
	v_mfma_f32_16x16x32_f16 v[110:113], v[190:193], v[158:161], v[110:113]
	v_mfma_f32_16x16x32_f16 v[102:105], v[198:201], v[158:161], v[102:105]
	v_mfma_f32_16x16x32_f16 v[94:97], v[190:193], v[150:153], v[94:97]
	v_mfma_f32_16x16x32_f16 v[82:85], v[198:201], v[150:153], v[82:85]
	v_mfma_f32_16x16x32_f16 v[130:133], v[194:197], v[178:181], v[130:133]
	v_mfma_f32_16x16x32_f16 v[126:129], v[202:205], v[178:181], v[126:129]
	v_mfma_f32_16x16x32_f16 v[122:125], v[194:197], v[170:173], v[122:125]
	v_mfma_f32_16x16x32_f16 v[118:121], v[202:205], v[170:173], v[118:121]
	v_mfma_f32_16x16x32_f16 v[110:113], v[194:197], v[162:165], v[110:113]
	v_mfma_f32_16x16x32_f16 v[102:105], v[202:205], v[162:165], v[102:105]
	v_mfma_f32_16x16x32_f16 v[94:97], v[194:197], v[154:157], v[94:97]
	v_mfma_f32_16x16x32_f16 v[82:85], v[202:205], v[154:157], v[82:85]
	s_setprio 0
	s_mov_b32 m0, s69
	v_lshl_add_u64 v[182:183], v[186:187], 0, s[30:31]
	s_barrier
	ds_read_b128 v[150:153], v237 offset:49152
	ds_read_b128 v[154:157], v237 offset:50176
	ds_read_b128 v[158:161], v237 offset:51200
	ds_read_b128 v[162:165], v237 offset:52224
	ds_read_b128 v[166:169], v237 offset:53248
	ds_read_b128 v[170:173], v237 offset:54272
	ds_read_b128 v[174:177], v237 offset:55296
	ds_read_b128 v[178:181], v237 offset:56320
	global_load_lds_dwordx4 v[182:183], off
	v_lshl_add_u64 v[182:183], v[188:189], 0, s[30:31]
	s_mov_b32 m0, s70
	s_nop 0
	global_load_lds_dwordx4 v[182:183], off
	s_barrier
	s_waitcnt lgkmcnt(0)
	s_setprio 1
	s_waitcnt lgkmcnt(0)
	v_mfma_f32_16x16x32_f16 v[70:73], v[134:137], v[150:153], v[70:73]
	v_mfma_f32_16x16x32_f16 v[58:61], v[142:145], v[150:153], v[58:61]
	v_mfma_f32_16x16x32_f16 v[50:53], v[134:137], v[158:161], v[50:53]
	v_mfma_f32_16x16x32_f16 v[38:41], v[142:145], v[158:161], v[38:41]
	v_mfma_f32_16x16x32_f16 v[26:29], v[134:137], v[166:169], v[26:29]
	v_mfma_f32_16x16x32_f16 v[18:21], v[142:145], v[166:169], v[18:21]
	v_mfma_f32_16x16x32_f16 v[10:13], v[134:137], v[174:177], v[10:13]
	v_mfma_f32_16x16x32_f16 v[6:9], v[142:145], v[174:177], v[6:9]
	v_mfma_f32_16x16x32_f16 v[70:73], v[138:141], v[154:157], v[70:73]
	v_mfma_f32_16x16x32_f16 v[58:61], v[146:149], v[154:157], v[58:61]
	v_mfma_f32_16x16x32_f16 v[50:53], v[138:141], v[162:165], v[50:53]
	v_mfma_f32_16x16x32_f16 v[38:41], v[146:149], v[162:165], v[38:41]
	v_mfma_f32_16x16x32_f16 v[26:29], v[138:141], v[170:173], v[26:29]
	v_mfma_f32_16x16x32_f16 v[18:21], v[146:149], v[170:173], v[18:21]
	v_mfma_f32_16x16x32_f16 v[10:13], v[138:141], v[178:181], v[10:13]
	v_mfma_f32_16x16x32_f16 v[6:9], v[146:149], v[178:181], v[6:9]
	s_setprio 0
	s_barrier
	s_add_u32 s44, s44, 0x40080
	s_addc_u32 s45, s45, 0
	s_mov_b32 m0, s50
	v_lshl_add_u64 v[134:135], s[44:45], 0, v[216:217]
	global_load_lds_dwordx4 v[134:135], off
	v_lshl_add_u64 v[134:135], s[44:45], 0, v[218:219]
	s_mov_b32 m0, s51
	s_nop 0
	global_load_lds_dwordx4 v[134:135], off
	s_waitcnt vmcnt(6)
	s_cmp_gt_i32 s61, 44
	s_cbranch_scc1 .Lhka_done_a3
	s_cmp_lt_i32 s61, 1
	s_cbranch_scc1 .Lhka_ld_a3
	s_add_i32 s94, s75, s61
	s_mov_b32 s95, 0
	s_cmpk_gt_u32 s94, 0x15ff
	s_cselect_b32 s97, 0x7fffea00, 0
	s_cselect_b32 s96, 0x80, 0
	s_add_i32 s97, s97, s94
	s_lshl_b32 s94, s97, 1
	s_add_i32 s97, s94, 0x2c00
	s_mul_hi_u32 s98, s97, 0xba2e8ba3
	s_lshr_b32 s98, s98, 11
	s_mul_i32 s99, s98, 0x7ffff500
	s_add_i32 s99, s99, s97
	s_lshr_b32 s97, s99, 7
	s_mul_i32 s98, s98, 22
	s_add_i32 s97, s97, s98
	s_lshl_b32 s97, s97, 8
	s_and_b32 s94, s94, 0x7e
	s_or_b32 s96, s97, s96
	s_or_b32 s94, s96, s94
	s_lshl_b64 s[96:97], s[94:95], 11
	v_cvt_pk_f16_f32 v2, v2, v3
	v_cvt_pk_f16_f32 v3, v4, v5
	v_lshl_add_u64 v[4:5], v[224:225], 0, s[96:97]
	global_store_dwordx2 v[4:5], v[2:3], off

.Lhka_done_a3:
	s_barrier
	s_setprio 1
	v_mfma_f32_16x16x32_f16 v[90:93], v[190:193], v[150:153], v[90:93]
	v_mfma_f32_16x16x32_f16 v[78:81], v[198:201], v[150:153], v[78:81]
	v_mfma_f32_16x16x32_f16 v[66:69], v[190:193], v[158:161], v[66:69]
	v_mfma_f32_16x16x32_f16 v[54:57], v[198:201], v[158:161], v[54:57]
	v_mfma_f32_16x16x32_f16 v[42:45], v[190:193], v[166:169], v[42:45]
	v_mfma_f32_16x16x32_f16 v[30:33], v[198:201], v[166:169], v[30:33]
	v_mfma_f32_16x16x32_f16 v[22:25], v[190:193], v[174:177], v[22:25]
	v_mfma_f32_16x16x32_f16 v[14:17], v[198:201], v[174:177], v[14:17]
	v_mfma_f32_16x16x32_f16 v[90:93], v[194:197], v[154:157], v[90:93]
	v_mfma_f32_16x16x32_f16 v[78:81], v[202:205], v[154:157], v[78:81]
	v_mfma_f32_16x16x32_f16 v[66:69], v[194:197], v[162:165], v[66:69]
	v_mfma_f32_16x16x32_f16 v[54:57], v[202:205], v[162:165], v[54:57]
	v_mfma_f32_16x16x32_f16 v[42:45], v[194:197], v[170:173], v[42:45]
	v_mfma_f32_16x16x32_f16 v[30:33], v[202:205], v[170:173], v[30:33]
	v_mfma_f32_16x16x32_f16 v[22:25], v[194:197], v[178:181], v[22:25]
	v_mfma_f32_16x16x32_f16 v[14:17], v[202:205], v[178:181], v[14:17]
	s_setprio 0
	s_add_i32 s28, s88, 2
	s_add_u32 s46, s46, 0x100
	s_addc_u32 s47, s47, 0
	s_add_u32 s86, s86, 0x100
	s_addc_u32 s87, s87, 0
	s_cmp_ge_i32 s88, s83
	s_barrier
	s_cbranch_scc1 .LBB4_49
	s_mov_b32 s88, s28
	s_branch .LBB4_32

.LBB5_18:
.LBB5_24:
	s_and_b64 s[46:47], s[38:39], exec
	s_cselect_b32 s48, s35, s43
	s_cselect_b32 s49, s34, s42
	s_cselect_b32 s50, s37, s41
	s_cselect_b32 s51, s36, s40
	s_add_u32 s24, s42, 0x100
	s_addc_u32 s80, s43, 0
	s_and_b64 s[46:47], s[44:45], exec
	s_cselect_b32 s47, s48, s80
	s_cselect_b32 s46, s49, s24
	s_add_u32 s24, s40, 0x100
	s_addc_u32 s80, s41, 0
	s_and_b64 s[44:45], s[44:45], exec
	s_cselect_b32 s45, s50, s80
	s_cselect_b32 s44, s51, s24
	s_mov_b32 m0, s55
	v_add_u32_e32 v227, s72, v232
	v_lshl_add_u64 v[130:131], s[44:45], 0, v[212:213]
	ds_read_b128 v[82:85], v227
	ds_read_b128 v[94:97], v227 offset:1024
	ds_read_b128 v[102:105], v227 offset:2048
	ds_read_b128 v[110:113], v227 offset:3072
	global_load_lds_dwordx4 v[130:131], off
	v_lshl_add_u64 v[132:133], s[44:45], 0, v[214:215]
	s_mov_b32 m0, s56
	s_nop 0
	global_load_lds_dwordx4 v[132:133], off
	s_barrier
	s_waitcnt lgkmcnt(0)
	s_setprio 1
	s_waitcnt lgkmcnt(0)
	v_mfma_f32_16x16x32_f16 v[90:93], v[82:85], v[46:49], 0
	v_mfma_f32_16x16x32_f16 v[46:49], v[102:105], v[46:49], 0
	v_mfma_f32_16x16x32_f16 v[90:93], v[94:97], v[50:53], v[90:93]
	v_mfma_f32_16x16x32_f16 v[46:49], v[110:113], v[50:53], v[46:49]
	v_mfma_f32_16x16x32_f16 v[50:53], v[82:85], v[38:41], 0
	v_mfma_f32_16x16x32_f16 v[38:41], v[102:105], v[38:41], 0
	v_mfma_f32_16x16x32_f16 v[106:109], v[110:113], v[42:45], v[38:41]
	v_mfma_f32_16x16x32_f16 v[38:41], v[82:85], v[30:33], 0
	v_mfma_f32_16x16x32_f16 v[30:33], v[102:105], v[30:33], 0
	v_mfma_f32_16x16x32_f16 v[170:173], v[110:113], v[34:37], v[30:33]
	v_mfma_f32_16x16x32_f16 v[30:33], v[82:85], v[22:25], 0
	v_mfma_f32_16x16x32_f16 v[22:25], v[102:105], v[22:25], 0
	v_mfma_f32_16x16x32_f16 v[98:101], v[94:97], v[42:45], v[50:53]
	v_mfma_f32_16x16x32_f16 v[166:169], v[94:97], v[34:37], v[38:41]
	v_mfma_f32_16x16x32_f16 v[174:177], v[94:97], v[26:29], v[30:33]
	v_mfma_f32_16x16x32_f16 v[178:181], v[110:113], v[26:29], v[22:25]
	s_setprio 0
	s_mov_b32 m0, s54
	s_barrier
	ds_read_b128 v[42:45], v235 offset:16384
	ds_read_b128 v[114:117], v235 offset:17408
	ds_read_b128 v[118:121], v235 offset:18432
	ds_read_b128 v[122:125], v235 offset:19456
	ds_read_b128 v[126:129], v235 offset:20480
	ds_read_b128 v[154:157], v235 offset:21504
	ds_read_b128 v[162:165], v235 offset:22528
	ds_read_b128 v[182:185], v235 offset:23552
	global_load_lds_dwordx4 v216, s[46:47]
	s_mov_b32 m0, s57
	s_nop 0
	global_load_lds_dwordx4 v222, s[46:47]
	s_barrier
	s_waitcnt lgkmcnt(0)
	s_setprio 1
	s_waitcnt lgkmcnt(0)
	v_mfma_f32_16x16x32_f16 v[22:25], v[6:9], v[42:45], 0
	v_mfma_f32_16x16x32_f16 v[30:33], v[6:9], v[118:121], 0
	v_mfma_f32_16x16x32_f16 v[38:41], v[6:9], v[126:129], 0
	v_mfma_f32_16x16x32_f16 v[6:9], v[6:9], v[162:165], 0
	v_mfma_f32_16x16x32_f16 v[22:25], v[10:13], v[114:117], v[22:25]
	v_mfma_f32_16x16x32_f16 v[26:29], v[14:17], v[42:45], 0
	v_mfma_f32_16x16x32_f16 v[30:33], v[10:13], v[122:125], v[30:33]
	v_mfma_f32_16x16x32_f16 v[34:37], v[14:17], v[118:121], 0
	v_mfma_f32_16x16x32_f16 v[38:41], v[10:13], v[154:157], v[38:41]
	v_mfma_f32_16x16x32_f16 v[50:53], v[14:17], v[126:129], 0
	v_mfma_f32_16x16x32_f16 v[6:9], v[10:13], v[182:185], v[6:9]
	v_mfma_f32_16x16x32_f16 v[10:13], v[14:17], v[162:165], 0
	v_mfma_f32_16x16x32_f16 v[26:29], v[18:21], v[114:117], v[26:29]
	v_mfma_f32_16x16x32_f16 v[34:37], v[18:21], v[122:125], v[34:37]
	v_mfma_f32_16x16x32_f16 v[50:53], v[18:21], v[154:157], v[50:53]
	v_mfma_f32_16x16x32_f16 v[14:17], v[18:21], v[182:185], v[10:13]
	s_setprio 0
	s_barrier
	s_add_u32 s82, s44, 0x40000
	s_addc_u32 s83, s45, 0
	s_add_i32 s80, s72, s53
	v_lshl_add_u64 v[10:11], s[82:83], 0, v[212:213]
	s_mov_b32 m0, s80
	s_add_i32 s81, s80, 0x2000
	global_load_lds_dwordx4 v[10:11], off
	v_lshl_add_u64 v[10:11], s[82:83], 0, v[214:215]
	s_mov_b32 m0, s81
	s_nop 0
	global_load_lds_dwordx4 v[10:11], off
	s_waitcnt vmcnt(6)
	s_cmp_gt_i32 s63, 44
	s_cbranch_scc1 .Lhkb_done_b0
	s_cmp_lt_i32 s63, 1
	s_cbranch_scc1 .Lhkb_ld_b0
	s_add_i32 s92, s71, s63
	s_mov_b32 s93, 0
	s_lshl_b64 s[90:91], s[92:93], 12
	v_cvt_pk_f16_f32 v2, v2, v3
	v_cvt_pk_f16_f32 v3, v4, v5
	v_lshl_add_u64 v[4:5], v[220:221], 0, s[90:91]
	global_store_dwordx2 v[4:5], v[2:3], off
.Lhkb_ld_b0:
	s_cmp_eq_u32 s63, 44
	s_cbranch_scc1 .Lhkb_inc_b0
	s_add_i32 s92, s63, s33
	s_mov_b32 s93, 0
	s_lshl_b64 s[90:91], s[92:93], 13
	v_lshl_add_u64 v[4:5], v[224:225], 0, s[90:91]
	global_load_dwordx4 v[2:5], v[4:5], off nt

.Lhkb_done_b0:
	s_barrier
	s_setprio 1
	v_mfma_f32_16x16x32_f16 v[10:13], v[82:85], v[42:45], 0
	v_mfma_f32_16x16x32_f16 v[134:137], v[94:97], v[114:117], v[10:13]
	v_mfma_f32_16x16x32_f16 v[10:13], v[102:105], v[42:45], 0
	v_mfma_f32_16x16x32_f16 v[138:141], v[110:113], v[114:117], v[10:13]
	v_mfma_f32_16x16x32_f16 v[10:13], v[82:85], v[118:121], 0
	v_mfma_f32_16x16x32_f16 v[142:145], v[94:97], v[122:125], v[10:13]
	v_mfma_f32_16x16x32_f16 v[10:13], v[102:105], v[118:121], 0
	v_mfma_f32_16x16x32_f16 v[146:149], v[110:113], v[122:125], v[10:13]
	v_mfma_f32_16x16x32_f16 v[10:13], v[82:85], v[126:129], 0
	v_mfma_f32_16x16x32_f16 v[150:153], v[94:97], v[154:157], v[10:13]
	v_mfma_f32_16x16x32_f16 v[10:13], v[102:105], v[126:129], 0
	v_mfma_f32_16x16x32_f16 v[154:157], v[110:113], v[154:157], v[10:13]
	v_mfma_f32_16x16x32_f16 v[10:13], v[82:85], v[162:165], 0
	v_mfma_f32_16x16x32_f16 v[158:161], v[94:97], v[182:185], v[10:13]
	v_mfma_f32_16x16x32_f16 v[10:13], v[102:105], v[162:165], 0
	v_mfma_f32_16x16x32_f16 v[162:165], v[110:113], v[182:185], v[10:13]
	s_setprio 0
	v_add_u32_e32 v229, 0x18000, v233
	s_barrier
	s_nop 3
	ds_read_b128 v[10:13], v229
	ds_read_b128 v[182:185], v229 offset:1024
	ds_read_b128 v[186:189], v229 offset:2048
	ds_read_b128 v[190:193], v229 offset:3072
	s_mov_b32 m0, s58
	ds_read_b128 v[122:125], v235 offset:32768
	ds_read_b128 v[126:129], v235 offset:33792
	ds_read_b128 v[114:117], v235 offset:34816
	ds_read_b128 v[206:209], v235 offset:35840
	ds_read_b128 v[198:201], v235 offset:36864
	ds_read_b128 v[202:205], v235 offset:37888
	ds_read_b128 v[18:21], v235 offset:38912
	ds_read_b128 v[194:197], v235 offset:39936
	global_load_lds_dwordx4 v226, s[46:47]
	s_mov_b32 m0, s59
	s_nop 0
	global_load_lds_dwordx4 v228, s[46:47]
	s_waitcnt lgkmcnt(8)
	s_barrier
	s_waitcnt lgkmcnt(0)
	s_setprio 1
	s_waitcnt lgkmcnt(0)
	v_mfma_f32_16x16x32_f16 v[42:45], v[10:13], v[122:125], v[54:57]
	v_mfma_f32_16x16x32_f16 v[118:121], v[182:185], v[126:129], v[42:45]
	v_mfma_f32_16x16x32_f16 v[42:45], v[186:189], v[122:125], v[58:61]
	v_mfma_f32_16x16x32_f16 v[110:113], v[190:193], v[126:129], v[42:45]
	v_mfma_f32_16x16x32_f16 v[42:45], v[10:13], v[114:117], v[62:65]
	v_mfma_f32_16x16x32_f16 v[102:105], v[182:185], v[206:209], v[42:45]
	v_mfma_f32_16x16x32_f16 v[42:45], v[186:189], v[114:117], v[66:69]
	v_mfma_f32_16x16x32_f16 v[94:97], v[190:193], v[206:209], v[42:45]
	v_mfma_f32_16x16x32_f16 v[42:45], v[10:13], v[198:201], v[70:73]
	v_mfma_f32_16x16x32_f16 v[82:85], v[182:185], v[202:205], v[42:45]
	v_mfma_f32_16x16x32_f16 v[42:45], v[186:189], v[198:201], v[74:77]
	v_mfma_f32_16x16x32_f16 v[66:69], v[190:193], v[202:205], v[42:45]
	v_mfma_f32_16x16x32_f16 v[42:45], v[10:13], v[18:21], v[78:81]
	v_mfma_f32_16x16x32_f16 v[54:57], v[182:185], v[194:197], v[42:45]
	v_mfma_f32_16x16x32_f16 v[42:45], v[186:189], v[18:21], v[86:89]
	v_mfma_f32_16x16x32_f16 v[42:45], v[190:193], v[194:197], v[42:45]
	s_setprio 0
	s_barrier
.LBB5_30:
	v_mov_b32_e32 v223, v217
	v_lshl_add_u64 v[58:59], s[46:47], 0, v[216:217]
	v_lshl_add_u64 v[60:61], s[46:47], 0, v[222:223]
	s_add_i32 s46, 0, 0x1c000
	s_mov_b32 m0, s62
	v_add_u32_e32 v236, s46, v232
	v_lshl_add_u64 v[62:63], v[130:131], 0, s[26:27]
	ds_read_b128 v[238:241], v236
	ds_read_b128 v[242:245], v236 offset:1024
	ds_read_b128 v[246:249], v236 offset:2048
	ds_read_b128 v[250:253], v236 offset:3072
	global_load_lds_dwordx4 v[62:63], off
	v_lshl_add_u64 v[62:63], v[132:133], 0, s[26:27]
	s_mov_b32 m0, s64
	s_nop 0
	global_load_lds_dwordx4 v[62:63], off
	s_barrier
	s_waitcnt lgkmcnt(0)
	s_setprio 1
	s_waitcnt lgkmcnt(0)
	v_mfma_f32_16x16x32_f16 v[62:65], v[238:241], v[122:125], v[90:93]
	v_mfma_f32_16x16x32_f16 v[46:49], v[246:249], v[122:125], v[46:49]
	v_mfma_f32_16x16x32_f16 v[130:133], v[242:245], v[126:129], v[62:65]
	v_mfma_f32_16x16x32_f16 v[126:129], v[250:253], v[126:129], v[46:49]
	v_mfma_f32_16x16x32_f16 v[46:49], v[238:241], v[114:117], v[98:101]
	v_mfma_f32_16x16x32_f16 v[122:125], v[242:245], v[206:209], v[46:49]
	v_mfma_f32_16x16x32_f16 v[46:49], v[246:249], v[114:117], v[106:109]
	v_mfma_f32_16x16x32_f16 v[114:117], v[250:253], v[206:209], v[46:49]
	v_mfma_f32_16x16x32_f16 v[46:49], v[238:241], v[198:201], v[166:169]
	v_mfma_f32_16x16x32_f16 v[106:109], v[242:245], v[202:205], v[46:49]
	v_mfma_f32_16x16x32_f16 v[46:49], v[246:249], v[198:201], v[170:173]
	v_mfma_f32_16x16x32_f16 v[98:101], v[250:253], v[202:205], v[46:49]
	v_mfma_f32_16x16x32_f16 v[46:49], v[238:241], v[18:21], v[174:177]
	v_mfma_f32_16x16x32_f16 v[18:21], v[246:249], v[18:21], v[178:181]
	v_mfma_f32_16x16x32_f16 v[90:93], v[242:245], v[194:197], v[46:49]
	v_mfma_f32_16x16x32_f16 v[78:81], v[250:253], v[194:197], v[18:21]
	s_setprio 0
	s_mov_b32 m0, s65
	s_nop 3
	v_lshl_add_u64 v[18:19], v[58:59], 0, s[26:27]
	s_barrier
	ds_read_b128 v[62:65], v235 offset:49152
	ds_read_b128 v[74:77], v235 offset:50176
	ds_read_b128 v[166:169], v235 offset:51200
	ds_read_b128 v[170:173], v235 offset:52224
	ds_read_b128 v[174:177], v235 offset:53248
	ds_read_b128 v[178:181], v235 offset:54272
	ds_read_b128 v[194:197], v235 offset:55296
	ds_read_b128 v[198:201], v235 offset:56320
	global_load_lds_dwordx4 v[18:19], off
	v_lshl_add_u64 v[18:19], v[60:61], 0, s[26:27]
	s_mov_b32 m0, s66
	s_nop 0
	global_load_lds_dwordx4 v[18:19], off
	s_barrier
	s_waitcnt lgkmcnt(0)
	s_setprio 1
	s_waitcnt lgkmcnt(0)
	v_mfma_f32_16x16x32_f16 v[18:21], v[10:13], v[62:65], v[22:25]
	v_mfma_f32_16x16x32_f16 v[70:73], v[182:185], v[74:77], v[18:21]
	v_mfma_f32_16x16x32_f16 v[18:21], v[186:189], v[62:65], v[26:29]
	v_mfma_f32_16x16x32_f16 v[58:61], v[190:193], v[74:77], v[18:21]
	v_mfma_f32_16x16x32_f16 v[18:21], v[10:13], v[166:169], v[30:33]
	v_mfma_f32_16x16x32_f16 v[46:49], v[182:185], v[170:173], v[18:21]
	v_mfma_f32_16x16x32_f16 v[18:21], v[186:189], v[166:169], v[34:37]
	v_mfma_f32_16x16x32_f16 v[34:37], v[190:193], v[170:173], v[18:21]
	v_mfma_f32_16x16x32_f16 v[18:21], v[10:13], v[174:177], v[38:41]
	v_mfma_f32_16x16x32_f16 v[6:9], v[10:13], v[194:197], v[6:9]
	v_mfma_f32_16x16x32_f16 v[26:29], v[182:185], v[178:181], v[18:21]
	v_mfma_f32_16x16x32_f16 v[18:21], v[186:189], v[174:177], v[50:53]
	v_mfma_f32_16x16x32_f16 v[10:13], v[182:185], v[198:201], v[6:9]
	v_mfma_f32_16x16x32_f16 v[6:9], v[186:189], v[194:197], v[14:17]
	v_mfma_f32_16x16x32_f16 v[18:21], v[190:193], v[178:181], v[18:21]
	v_mfma_f32_16x16x32_f16 v[6:9], v[190:193], v[198:201], v[6:9]
	s_setprio 0
	s_barrier
	s_add_u32 s44, s44, 0x40080
	s_addc_u32 s45, s45, 0
	s_add_i32 s46, s46, s53
	v_lshl_add_u64 v[14:15], s[44:45], 0, v[212:213]
	s_mov_b32 m0, s46
	s_add_i32 s47, s46, 0x2000
	global_load_lds_dwordx4 v[14:15], off
	v_lshl_add_u64 v[14:15], s[44:45], 0, v[214:215]
	s_mov_b32 m0, s47
	s_nop 0
	global_load_lds_dwordx4 v[14:15], off
	s_waitcnt vmcnt(6)
	s_cmp_gt_i32 s63, 44
	s_cbranch_scc1 .Lhkb_done_b1
	s_cmp_lt_i32 s63, 1
	s_cbranch_scc1 .Lhkb_ld_b1
	s_add_i32 s92, s71, s63
	s_mov_b32 s93, 0
	s_lshl_b64 s[90:91], s[92:93], 12
	v_cvt_pk_f16_f32 v2, v2, v3
	v_cvt_pk_f16_f32 v3, v4, v5
	v_lshl_add_u64 v[4:5], v[220:221], 0, s[90:91]
	global_store_dwordx2 v[4:5], v[2:3], off

.Lhkb_done_b1:
	s_barrier
	s_setprio 1
	v_mfma_f32_16x16x32_f16 v[14:17], v[238:241], v[62:65], v[134:137]
	v_mfma_f32_16x16x32_f16 v[86:89], v[242:245], v[74:77], v[14:17]
	v_mfma_f32_16x16x32_f16 v[14:17], v[246:249], v[62:65], v[138:141]
	v_mfma_f32_16x16x32_f16 v[74:77], v[250:253], v[74:77], v[14:17]
	v_mfma_f32_16x16x32_f16 v[14:17], v[238:241], v[166:169], v[142:145]
	v_mfma_f32_16x16x32_f16 v[62:65], v[242:245], v[170:173], v[14:17]
	v_mfma_f32_16x16x32_f16 v[14:17], v[246:249], v[166:169], v[146:149]
	v_mfma_f32_16x16x32_f16 v[50:53], v[250:253], v[170:173], v[14:17]
	v_mfma_f32_16x16x32_f16 v[14:17], v[238:241], v[174:177], v[150:153]
	v_mfma_f32_16x16x32_f16 v[38:41], v[242:245], v[178:181], v[14:17]
	v_mfma_f32_16x16x32_f16 v[14:17], v[246:249], v[174:177], v[154:157]
	v_mfma_f32_16x16x32_f16 v[30:33], v[250:253], v[178:181], v[14:17]
	v_mfma_f32_16x16x32_f16 v[14:17], v[238:241], v[194:197], v[158:161]
	v_mfma_f32_16x16x32_f16 v[22:25], v[242:245], v[198:201], v[14:17]
	v_mfma_f32_16x16x32_f16 v[14:17], v[246:249], v[194:197], v[162:165]
	v_mfma_f32_16x16x32_f16 v[14:17], v[250:253], v[198:201], v[14:17]
	s_setprio 0
	s_cmp_lt_u32 s79, 3
	s_barrier
	s_cbranch_scc1 .LBB5_49
	s_add_u32 s42, s42, 0x180
	s_addc_u32 s43, s43, 0
	s_add_u32 s82, s40, 0x200
	s_addc_u32 s83, s41, 0
	s_mov_b32 s84, 4

.LBB5_40:
	s_add_u32 s24, s42, 0x80
	s_addc_u32 s44, s43, 0
	s_and_b64 s[40:41], s[40:41], exec
	s_cselect_b32 s41, s50, s83
	s_cselect_b32 s40, s51, s82
	s_mov_b32 m0, s55
	v_lshl_add_u64 v[182:183], s[40:41], 0, v[212:213]
	ds_read_b128 v[186:189], v227
	ds_read_b128 v[190:193], v227 offset:1024
	ds_read_b128 v[194:197], v227 offset:2048
	ds_read_b128 v[198:201], v227 offset:3072
	global_load_lds_dwordx4 v[182:183], off
	v_lshl_add_u64 v[184:185], s[40:41], 0, v[214:215]
	s_mov_b32 m0, s56
	s_cselect_b32 s45, s48, s44
	global_load_lds_dwordx4 v[184:185], off
	s_barrier
	s_waitcnt lgkmcnt(0)
	s_cselect_b32 s44, s49, s24
	s_setprio 1
	s_waitcnt lgkmcnt(0)
	v_mfma_f32_16x16x32_f16 v[130:133], v[186:189], v[174:177], v[130:133]
	v_mfma_f32_16x16x32_f16 v[126:129], v[194:197], v[174:177], v[126:129]
	v_mfma_f32_16x16x32_f16 v[122:125], v[186:189], v[166:169], v[122:125]
	v_mfma_f32_16x16x32_f16 v[114:117], v[194:197], v[166:169], v[114:117]
	v_mfma_f32_16x16x32_f16 v[106:109], v[186:189], v[158:161], v[106:109]
	v_mfma_f32_16x16x32_f16 v[98:101], v[194:197], v[158:161], v[98:101]
	v_mfma_f32_16x16x32_f16 v[90:93], v[186:189], v[150:153], v[90:93]
	v_mfma_f32_16x16x32_f16 v[78:81], v[194:197], v[150:153], v[78:81]
	v_mfma_f32_16x16x32_f16 v[130:133], v[190:193], v[178:181], v[130:133]
	v_mfma_f32_16x16x32_f16 v[126:129], v[198:201], v[178:181], v[126:129]
	v_mfma_f32_16x16x32_f16 v[122:125], v[190:193], v[170:173], v[122:125]
	v_mfma_f32_16x16x32_f16 v[114:117], v[198:201], v[170:173], v[114:117]
	v_mfma_f32_16x16x32_f16 v[106:109], v[190:193], v[162:165], v[106:109]
	v_mfma_f32_16x16x32_f16 v[98:101], v[198:201], v[162:165], v[98:101]
	v_mfma_f32_16x16x32_f16 v[90:93], v[190:193], v[154:157], v[90:93]
	v_mfma_f32_16x16x32_f16 v[78:81], v[198:201], v[154:157], v[78:81]
	s_setprio 0
	s_mov_b32 m0, s54
	s_barrier
	ds_read_b128 v[150:153], v235 offset:16384
	ds_read_b128 v[154:157], v235 offset:17408
	ds_read_b128 v[158:161], v235 offset:18432
	ds_read_b128 v[162:165], v235 offset:19456
	ds_read_b128 v[166:169], v235 offset:20480
	ds_read_b128 v[170:173], v235 offset:21504
	ds_read_b128 v[174:177], v235 offset:22528
	ds_read_b128 v[178:181], v235 offset:23552
	global_load_lds_dwordx4 v216, s[44:45]
	s_mov_b32 m0, s57
	s_nop 0
	global_load_lds_dwordx4 v222, s[44:45]
	s_barrier
	s_waitcnt lgkmcnt(0)
	s_setprio 1
	s_waitcnt lgkmcnt(0)
	v_mfma_f32_16x16x32_f16 v[70:73], v[134:137], v[150:153], v[70:73]
	v_mfma_f32_16x16x32_f16 v[58:61], v[142:145], v[150:153], v[58:61]
	v_mfma_f32_16x16x32_f16 v[46:49], v[134:137], v[158:161], v[46:49]
	v_mfma_f32_16x16x32_f16 v[34:37], v[142:145], v[158:161], v[34:37]
	v_mfma_f32_16x16x32_f16 v[26:29], v[134:137], v[166:169], v[26:29]
	v_mfma_f32_16x16x32_f16 v[18:21], v[142:145], v[166:169], v[18:21]
	v_mfma_f32_16x16x32_f16 v[10:13], v[134:137], v[174:177], v[10:13]
	v_mfma_f32_16x16x32_f16 v[6:9], v[142:145], v[174:177], v[6:9]
	v_mfma_f32_16x16x32_f16 v[70:73], v[138:141], v[154:157], v[70:73]
	v_mfma_f32_16x16x32_f16 v[58:61], v[146:149], v[154:157], v[58:61]
	v_mfma_f32_16x16x32_f16 v[46:49], v[138:141], v[162:165], v[46:49]
	v_mfma_f32_16x16x32_f16 v[34:37], v[146:149], v[162:165], v[34:37]
	v_mfma_f32_16x16x32_f16 v[26:29], v[138:141], v[170:173], v[26:29]
	v_mfma_f32_16x16x32_f16 v[18:21], v[146:149], v[170:173], v[18:21]
	v_mfma_f32_16x16x32_f16 v[10:13], v[138:141], v[178:181], v[10:13]
	v_mfma_f32_16x16x32_f16 v[6:9], v[146:149], v[178:181], v[6:9]
	s_setprio 0
	s_barrier
	s_add_u32 s86, s40, 0x40000
	s_addc_u32 s87, s41, 0
	s_mov_b32 m0, s80
	v_lshl_add_u64 v[134:135], s[86:87], 0, v[212:213]
	global_load_lds_dwordx4 v[134:135], off
	v_lshl_add_u64 v[134:135], s[86:87], 0, v[214:215]
	s_mov_b32 m0, s81
	s_nop 0
	global_load_lds_dwordx4 v[134:135], off
	s_waitcnt vmcnt(6)
	s_cmp_gt_i32 s63, 44
	s_cbranch_scc1 .Lhkb_done_b2
	s_cmp_lt_i32 s63, 1
	s_cbranch_scc1 .Lhkb_ld_b2
	s_add_i32 s92, s71, s63
	s_mov_b32 s93, 0
	s_lshl_b64 s[90:91], s[92:93], 12
	v_cvt_pk_f16_f32 v2, v2, v3
	v_cvt_pk_f16_f32 v3, v4, v5
	v_lshl_add_u64 v[4:5], v[220:221], 0, s[90:91]
	global_store_dwordx2 v[4:5], v[2:3], off

.Lhkb_done_b2:
	s_barrier
	s_setprio 1
	v_mfma_f32_16x16x32_f16 v[86:89], v[186:189], v[150:153], v[86:89]
	v_mfma_f32_16x16x32_f16 v[74:77], v[194:197], v[150:153], v[74:77]
	v_mfma_f32_16x16x32_f16 v[62:65], v[186:189], v[158:161], v[62:65]
	v_mfma_f32_16x16x32_f16 v[50:53], v[194:197], v[158:161], v[50:53]
	v_mfma_f32_16x16x32_f16 v[38:41], v[186:189], v[166:169], v[38:41]
	v_mfma_f32_16x16x32_f16 v[30:33], v[194:197], v[166:169], v[30:33]
	v_mfma_f32_16x16x32_f16 v[22:25], v[186:189], v[174:177], v[22:25]
	v_mfma_f32_16x16x32_f16 v[14:17], v[194:197], v[174:177], v[14:17]
	v_mfma_f32_16x16x32_f16 v[86:89], v[190:193], v[154:157], v[86:89]
	v_mfma_f32_16x16x32_f16 v[74:77], v[198:201], v[154:157], v[74:77]
	v_mfma_f32_16x16x32_f16 v[62:65], v[190:193], v[162:165], v[62:65]
	v_mfma_f32_16x16x32_f16 v[50:53], v[198:201], v[162:165], v[50:53]
	v_mfma_f32_16x16x32_f16 v[38:41], v[190:193], v[170:173], v[38:41]
	v_mfma_f32_16x16x32_f16 v[30:33], v[198:201], v[170:173], v[30:33]
	v_mfma_f32_16x16x32_f16 v[22:25], v[190:193], v[178:181], v[22:25]
	v_mfma_f32_16x16x32_f16 v[14:17], v[198:201], v[178:181], v[14:17]
	s_setprio 0
	s_barrier
	ds_read_b128 v[134:137], v229
	ds_read_b128 v[138:141], v229 offset:1024
	ds_read_b128 v[142:145], v229 offset:2048
	ds_read_b128 v[146:149], v229 offset:3072
	s_mov_b32 m0, s58
	ds_read_b128 v[174:177], v235 offset:32768
	ds_read_b128 v[178:181], v235 offset:33792
	ds_read_b128 v[166:169], v235 offset:34816
	ds_read_b128 v[170:173], v235 offset:35840
	ds_read_b128 v[158:161], v235 offset:36864
	ds_read_b128 v[162:165], v235 offset:37888
	ds_read_b128 v[150:153], v235 offset:38912
	ds_read_b128 v[154:157], v235 offset:39936
	global_load_lds_dwordx4 v226, s[44:45]
	s_mov_b32 m0, s59
	s_nop 0
	global_load_lds_dwordx4 v228, s[44:45]
	s_waitcnt lgkmcnt(8)
	s_barrier
	s_waitcnt lgkmcnt(0)
	s_setprio 1
	s_waitcnt lgkmcnt(0)
	v_mfma_f32_16x16x32_f16 v[118:121], v[134:137], v[174:177], v[118:121]
	v_mfma_f32_16x16x32_f16 v[110:113], v[142:145], v[174:177], v[110:113]
	v_mfma_f32_16x16x32_f16 v[102:105], v[134:137], v[166:169], v[102:105]
	v_mfma_f32_16x16x32_f16 v[94:97], v[142:145], v[166:169], v[94:97]
	v_mfma_f32_16x16x32_f16 v[82:85], v[134:137], v[158:161], v[82:85]
	v_mfma_f32_16x16x32_f16 v[66:69], v[142:145], v[158:161], v[66:69]
	v_mfma_f32_16x16x32_f16 v[54:57], v[134:137], v[150:153], v[54:57]
	v_mfma_f32_16x16x32_f16 v[42:45], v[142:145], v[150:153], v[42:45]
	v_mfma_f32_16x16x32_f16 v[118:121], v[138:141], v[178:181], v[118:121]
	v_mfma_f32_16x16x32_f16 v[110:113], v[146:149], v[178:181], v[110:113]
	v_mfma_f32_16x16x32_f16 v[102:105], v[138:141], v[170:173], v[102:105]
	v_mfma_f32_16x16x32_f16 v[94:97], v[146:149], v[170:173], v[94:97]
	v_mfma_f32_16x16x32_f16 v[82:85], v[138:141], v[162:165], v[82:85]
	v_mfma_f32_16x16x32_f16 v[66:69], v[146:149], v[162:165], v[66:69]
	v_mfma_f32_16x16x32_f16 v[54:57], v[138:141], v[154:157], v[54:57]
	v_mfma_f32_16x16x32_f16 v[42:45], v[146:149], v[154:157], v[42:45]
	s_setprio 0
	s_barrier
.LBB5_46:
	s_mov_b32 m0, s62
	v_lshl_add_u64 v[182:183], v[182:183], 0, s[26:27]
	ds_read_b128 v[190:193], v236
	ds_read_b128 v[194:197], v236 offset:1024
	ds_read_b128 v[198:201], v236 offset:2048
	ds_read_b128 v[202:205], v236 offset:3072
	global_load_lds_dwordx4 v[182:183], off
	v_lshl_add_u64 v[182:183], v[184:185], 0, s[26:27]
	s_mov_b32 m0, s64
	v_mov_b32_e32 v223, v217
	global_load_lds_dwordx4 v[182:183], off
	s_barrier
	s_waitcnt lgkmcnt(0)
	v_lshl_add_u64 v[186:187], s[44:45], 0, v[216:217]
	v_lshl_add_u64 v[188:189], s[44:45], 0, v[222:223]
	s_setprio 1
	s_waitcnt lgkmcnt(0)
	v_mfma_f32_16x16x32_f16 v[130:133], v[190:193], v[174:177], v[130:133]
	v_mfma_f32_16x16x32_f16 v[126:129], v[198:201], v[174:177], v[126:129]
	v_mfma_f32_16x16x32_f16 v[122:125], v[190:193], v[166:169], v[122:125]
	v_mfma_f32_16x16x32_f16 v[114:117], v[198:201], v[166:169], v[114:117]
	v_mfma_f32_16x16x32_f16 v[106:109], v[190:193], v[158:161], v[106:109]
	v_mfma_f32_16x16x32_f16 v[98:101], v[198:201], v[158:161], v[98:101]
	v_mfma_f32_16x16x32_f16 v[90:93], v[190:193], v[150:153], v[90:93]
	v_mfma_f32_16x16x32_f16 v[78:81], v[198:201], v[150:153], v[78:81]
	v_mfma_f32_16x16x32_f16 v[130:133], v[194:197], v[178:181], v[130:133]
	v_mfma_f32_16x16x32_f16 v[126:129], v[202:205], v[178:181], v[126:129]
	v_mfma_f32_16x16x32_f16 v[122:125], v[194:197], v[170:173], v[122:125]
	v_mfma_f32_16x16x32_f16 v[114:117], v[202:205], v[170:173], v[114:117]
	v_mfma_f32_16x16x32_f16 v[106:109], v[194:197], v[162:165], v[106:109]
	v_mfma_f32_16x16x32_f16 v[98:101], v[202:205], v[162:165], v[98:101]
	v_mfma_f32_16x16x32_f16 v[90:93], v[194:197], v[154:157], v[90:93]
	v_mfma_f32_16x16x32_f16 v[78:81], v[202:205], v[154:157], v[78:81]
	s_setprio 0
	s_mov_b32 m0, s65
	v_lshl_add_u64 v[182:183], v[186:187], 0, s[26:27]
	s_barrier
	ds_read_b128 v[150:153], v235 offset:49152
	ds_read_b128 v[154:157], v235 offset:50176
	ds_read_b128 v[158:161], v235 offset:51200
	ds_read_b128 v[162:165], v235 offset:52224
	ds_read_b128 v[166:169], v235 offset:53248
	ds_read_b128 v[170:173], v235 offset:54272
	ds_read_b128 v[174:177], v235 offset:55296
	ds_read_b128 v[178:181], v235 offset:56320
	global_load_lds_dwordx4 v[182:183], off
	v_lshl_add_u64 v[182:183], v[188:189], 0, s[26:27]
	s_mov_b32 m0, s66
	s_nop 0
	global_load_lds_dwordx4 v[182:183], off
	s_barrier
	s_waitcnt lgkmcnt(0)
	s_setprio 1
	s_waitcnt lgkmcnt(0)
	v_mfma_f32_16x16x32_f16 v[70:73], v[134:137], v[150:153], v[70:73]
	v_mfma_f32_16x16x32_f16 v[58:61], v[142:145], v[150:153], v[58:61]
	v_mfma_f32_16x16x32_f16 v[46:49], v[134:137], v[158:161], v[46:49]
	v_mfma_f32_16x16x32_f16 v[34:37], v[142:145], v[158:161], v[34:37]
	v_mfma_f32_16x16x32_f16 v[26:29], v[134:137], v[166:169], v[26:29]
	v_mfma_f32_16x16x32_f16 v[18:21], v[142:145], v[166:169], v[18:21]
	v_mfma_f32_16x16x32_f16 v[10:13], v[134:137], v[174:177], v[10:13]
	v_mfma_f32_16x16x32_f16 v[6:9], v[142:145], v[174:177], v[6:9]
	v_mfma_f32_16x16x32_f16 v[70:73], v[138:141], v[154:157], v[70:73]
	v_mfma_f32_16x16x32_f16 v[58:61], v[146:149], v[154:157], v[58:61]
	v_mfma_f32_16x16x32_f16 v[46:49], v[138:141], v[162:165], v[46:49]
	v_mfma_f32_16x16x32_f16 v[34:37], v[146:149], v[162:165], v[34:37]
	v_mfma_f32_16x16x32_f16 v[26:29], v[138:141], v[170:173], v[26:29]
	v_mfma_f32_16x16x32_f16 v[18:21], v[146:149], v[170:173], v[18:21]
	v_mfma_f32_16x16x32_f16 v[10:13], v[138:141], v[178:181], v[10:13]
	v_mfma_f32_16x16x32_f16 v[6:9], v[146:149], v[178:181], v[6:9]
	s_setprio 0
	s_barrier
	s_add_u32 s40, s40, 0x40080
	s_addc_u32 s41, s41, 0
	s_mov_b32 m0, s46
	v_lshl_add_u64 v[134:135], s[40:41], 0, v[212:213]
	global_load_lds_dwordx4 v[134:135], off
	v_lshl_add_u64 v[134:135], s[40:41], 0, v[214:215]
	s_mov_b32 m0, s47
	s_nop 0
	global_load_lds_dwordx4 v[134:135], off
	s_waitcnt vmcnt(6)
	s_cmp_gt_i32 s63, 44
	s_cbranch_scc1 .Lhkb_done_b3
	s_cmp_lt_i32 s63, 1
	s_cbranch_scc1 .Lhkb_ld_b3
	s_add_i32 s92, s71, s63
	s_mov_b32 s93, 0
	s_lshl_b64 s[90:91], s[92:93], 12
	v_cvt_pk_f16_f32 v2, v2, v3
	v_cvt_pk_f16_f32 v3, v4, v5
	v_lshl_add_u64 v[4:5], v[220:221], 0, s[90:91]
	global_store_dwordx2 v[4:5], v[2:3], off

.Lhkb_done_b3:
	s_barrier
	s_setprio 1
	v_mfma_f32_16x16x32_f16 v[86:89], v[190:193], v[150:153], v[86:89]
	v_mfma_f32_16x16x32_f16 v[74:77], v[198:201], v[150:153], v[74:77]
	v_mfma_f32_16x16x32_f16 v[62:65], v[190:193], v[158:161], v[62:65]
	v_mfma_f32_16x16x32_f16 v[50:53], v[198:201], v[158:161], v[50:53]
	v_mfma_f32_16x16x32_f16 v[38:41], v[190:193], v[166:169], v[38:41]
	v_mfma_f32_16x16x32_f16 v[30:33], v[198:201], v[166:169], v[30:33]
	v_mfma_f32_16x16x32_f16 v[22:25], v[190:193], v[174:177], v[22:25]
	v_mfma_f32_16x16x32_f16 v[14:17], v[198:201], v[174:177], v[14:17]
	v_mfma_f32_16x16x32_f16 v[86:89], v[194:197], v[154:157], v[86:89]
	v_mfma_f32_16x16x32_f16 v[74:77], v[202:205], v[154:157], v[74:77]
	v_mfma_f32_16x16x32_f16 v[62:65], v[194:197], v[162:165], v[62:65]
	v_mfma_f32_16x16x32_f16 v[50:53], v[202:205], v[162:165], v[50:53]
	v_mfma_f32_16x16x32_f16 v[38:41], v[194:197], v[170:173], v[38:41]
	v_mfma_f32_16x16x32_f16 v[30:33], v[202:205], v[170:173], v[30:33]
	v_mfma_f32_16x16x32_f16 v[22:25], v[194:197], v[178:181], v[22:25]
	v_mfma_f32_16x16x32_f16 v[14:17], v[202:205], v[178:181], v[14:17]
	s_setprio 0
	s_add_i32 s24, s84, 2
	s_add_u32 s42, s42, 0x100
	s_addc_u32 s43, s43, 0
	s_add_u32 s82, s82, 0x100
	s_addc_u32 s83, s83, 0
	s_cmp_ge_i32 s84, s79
	s_barrier
	s_cbranch_scc1 .LBB5_49
	s_mov_b32 s84, s24
	s_branch .LBB5_32

	.amdhsa_kernel _Z7k_gemm1ILi1EEvPKDF16_S1_PDF16_PK15HIP_vector_typeIiLj2EEPKfS8_S2_PKt
		.amdhsa_group_segment_fixed_size 0
		.amdhsa_private_segment_fixed_size 0
		.amdhsa_kernarg_size 64
		.amdhsa_user_sgpr_count 2
		.amdhsa_user_sgpr_dispatch_ptr 0
		.amdhsa_user_sgpr_queue_ptr 0
		.amdhsa_user_sgpr_kernarg_segment_ptr 1
		.amdhsa_user_sgpr_dispatch_id 0
		.amdhsa_user_sgpr_kernarg_preload_length 0
		.amdhsa_user_sgpr_kernarg_preload_offset 0
		.amdhsa_user_sgpr_private_segment_size 0
		.amdhsa_uses_dynamic_stack 0
		.amdhsa_enable_private_segment 0
		.amdhsa_system_sgpr_workgroup_id_x 1
		.amdhsa_system_sgpr_workgroup_id_y 0
		.amdhsa_system_sgpr_workgroup_id_z 0
		.amdhsa_system_sgpr_workgroup_info 0
		.amdhsa_system_vgpr_workitem_id 0
		.amdhsa_next_free_vgpr 254
		.amdhsa_next_free_sgpr 94
		.amdhsa_accum_offset 256
		.amdhsa_reserve_vcc 1
		.amdhsa_float_round_mode_32 0
		.amdhsa_float_round_mode_16_64 0
		.amdhsa_float_denorm_mode_32 3
		.amdhsa_float_denorm_mode_16_64 3
		.amdhsa_dx10_clamp 1
		.amdhsa_ieee_mode 1
		.amdhsa_fp16_overflow 0
		.amdhsa_tg_split 0
		.amdhsa_exception_fp_ieee_invalid_op 0
		.amdhsa_exception_fp_denorm_src 0
		.amdhsa_exception_fp_ieee_div_zero 0
		.amdhsa_exception_fp_ieee_overflow 0
		.amdhsa_exception_fp_ieee_underflow 0
		.amdhsa_exception_fp_ieee_inexact 0
		.amdhsa_exception_int_div_zero 0
	.end_amdhsa_kernel

amdhsa.kernels:
  - .agpr_count:     0
    .args:
      - .actual_access:  read_only
        .address_space:  global
        .offset:         0
        .size:           8
        .value_kind:     global_buffer
      - .actual_access:  read_only
        .address_space:  global
        .offset:         8
        .size:           8
        .value_kind:     global_buffer
      - .actual_access:  write_only
        .address_space:  global
        .offset:         16
        .size:           8
        .value_kind:     global_buffer
      - .actual_access:  write_only
        .address_space:  global
        .offset:         24
        .size:           8
        .value_kind:     global_buffer
      - .actual_access:  write_only
        .address_space:  global
        .offset:         32
        .size:           8
        .value_kind:     global_buffer
      - .actual_access:  write_only
        .address_space:  global
        .offset:         40
        .size:           8
        .value_kind:     global_buffer
    .group_segment_fixed_size: 256
    .kernarg_segment_align: 8
    .kernarg_segment_size: 48
    .language:       OpenCL C
    .language_version:
      - 2
      - 0
    .max_flat_workgroup_size: 256
    .name:           _Z10k_xscatterPKiS0_P15HIP_vector_typeIiLj2EEPtP4MetaS3_
    .private_segment_fixed_size: 0
    .sgpr_count:     41
    .sgpr_spill_count: 0
    .symbol:         _Z10k_xscatterPKiS0_P15HIP_vector_typeIiLj2EEPtP4MetaS3_.kd
    .uniform_work_group_size: 1
    .uses_dynamic_stack: false
    .vgpr_count:     55
    .vgpr_spill_count: 0
    .wavefront_size: 64
  - .agpr_count:     0
    .args:
      - .actual_access:  read_only
        .address_space:  global
        .offset:         0
        .size:           8
        .value_kind:     global_buffer
      - .actual_access:  read_only
        .address_space:  global
        .offset:         8
        .size:           8
        .value_kind:     global_buffer
      - .actual_access:  write_only
        .address_space:  global
        .offset:         16
        .size:           8
        .value_kind:     global_buffer
      - .actual_access:  write_only
        .address_space:  global
        .offset:         24
        .size:           8
        .value_kind:     global_buffer
      - .actual_access:  write_only
        .address_space:  global
        .offset:         32
        .size:           8
        .value_kind:     global_buffer
      - .actual_access:  read_only
        .address_space:  global
        .offset:         40
        .size:           8
        .value_kind:     global_buffer
      - .actual_access:  read_only
        .address_space:  global
        .offset:         48
        .size:           8
        .value_kind:     global_buffer
      - .actual_access:  write_only
        .address_space:  global
        .offset:         56
        .size:           8
        .value_kind:     global_buffer
      - .actual_access:  write_only
        .address_space:  global
        .offset:         64
        .size:           8
        .value_kind:     global_buffer
    .group_segment_fixed_size: 4096
    .kernarg_segment_align: 8
    .kernarg_segment_size: 72
    .language:       OpenCL C
    .language_version:
      - 2
      - 0
    .max_flat_workgroup_size: 256
    .name:           _Z5k_prePKfS0_PiP15HIP_vector_typeIfLj2EES1_S0_S0_PDF16_S5_
    .private_segment_fixed_size: 0
    .sgpr_count:     42
    .sgpr_spill_count: 0
    .symbol:         _Z5k_prePKfS0_PiP15HIP_vector_typeIfLj2EES1_S0_S0_PDF16_S5_.kd
    .uniform_work_group_size: 1
    .uses_dynamic_stack: false
    .vgpr_count:     128
    .vgpr_spill_count: 0
    .wavefront_size: 64
  - .agpr_count:     0
    .args:
      - .address_space:  global
        .offset:         0
        .size:           8
        .value_kind:     global_buffer
      - .address_space:  global
        .offset:         8
        .size:           8
        .value_kind:     global_buffer
      - .actual_access:  write_only
        .address_space:  global
        .offset:         16
        .size:           8
        .value_kind:     global_buffer
      - .actual_access:  read_only
        .address_space:  global
        .offset:         24
        .size:           8
        .value_kind:     global_buffer
    .group_segment_fixed_size: 0
    .kernarg_segment_align: 8
    .kernarg_segment_size: 32
    .language:       OpenCL C
    .language_version:
      - 2
      - 0
    .max_flat_workgroup_size: 512
    .name:           _Z7k_gemm2PKDF16_S0_PDF16_PK15HIP_vector_typeIiLj2EE
    .private_segment_fixed_size: 0
    .sgpr_count:     74
    .sgpr_spill_count: 0
    .symbol:         _Z7k_gemm2PKDF16_S0_PDF16_PK15HIP_vector_typeIiLj2EE.kd
    .uniform_work_group_size: 1
    .uses_dynamic_stack: false
    .vgpr_count:     226
    .vgpr_spill_count: 0
    .wavefront_size: 64
  - .agpr_count:     0
    .args:
      - .actual_access:  read_only
        .address_space:  global
        .offset:         0
        .size:           8
        .value_kind:     global_buffer
      - .actual_access:  read_only
        .address_space:  global
        .offset:         8
        .size:           8
        .value_kind:     global_buffer
      - .actual_access:  read_only
        .address_space:  global
        .offset:         16
        .size:           8
        .value_kind:     global_buffer
      - .actual_access:  write_only
        .address_space:  global
        .offset:         24
        .size:           8
        .value_kind:     global_buffer
    .group_segment_fixed_size: 0
    .kernarg_segment_align: 8
    .kernarg_segment_size: 32
    .language:       OpenCL C
    .language_version:
      - 2
      - 0
    .max_flat_workgroup_size: 256
    .name:           _Z9k_combinePKDF16_PK15HIP_vector_typeIiLj2EEPKS1_IfLj2EEPf
    .private_segment_fixed_size: 0
    .sgpr_count:     30
    .sgpr_spill_count: 0
    .symbol:         _Z9k_combinePKDF16_PK15HIP_vector_typeIiLj2EEPKS1_IfLj2EEPf.kd
    .uniform_work_group_size: 1
    .uses_dynamic_stack: false
    .vgpr_count:     64
    .vgpr_spill_count: 0
    .wavefront_size: 64
  - .agpr_count:     0
    .args:
      - .address_space:  global
        .offset:         0
        .size:           8
        .value_kind:     global_buffer
      - .address_space:  global
        .offset:         8
        .size:           8
        .value_kind:     global_buffer
      - .actual_access:  write_only
        .address_space:  global
        .offset:         16
        .size:           8
        .value_kind:     global_buffer
      - .actual_access:  read_only
        .address_space:  global
        .offset:         24
        .size:           8
        .value_kind:     global_buffer
      - .address_space:  global
        .offset:         32
        .size:           8
        .value_kind:     global_buffer
      - .address_space:  global
        .offset:         40
        .size:           8
        .value_kind:     global_buffer
      - .actual_access:  write_only
        .address_space:  global
        .offset:         48
        .size:           8
        .value_kind:     global_buffer
      - .address_space:  global
        .offset:         56
        .size:           8
        .value_kind:     global_buffer
    .group_segment_fixed_size: 0
    .kernarg_segment_align: 8
    .kernarg_segment_size: 64
    .language:       OpenCL C
    .language_version:
      - 2
      - 0
    .max_flat_workgroup_size: 512
    .name:           _Z7k_gemm1ILi0EEvPKDF16_S1_PDF16_PK15HIP_vector_typeIiLj2EEPKfS8_S2_PKt
    .private_segment_fixed_size: 0
    .sgpr_count:     106
    .sgpr_spill_count: 0
    .symbol:         _Z7k_gemm1ILi0EEvPKDF16_S1_PDF16_PK15HIP_vector_typeIiLj2EEPKfS8_S2_PKt.kd
    .uniform_work_group_size: 1
    .uses_dynamic_stack: false
    .vgpr_count:     256
    .vgpr_spill_count: 0
    .wavefront_size: 64
  - .agpr_count:     0
    .args:
      - .address_space:  global
        .offset:         0
        .size:           8
        .value_kind:     global_buffer
      - .address_space:  global
        .offset:         8
        .size:           8
        .value_kind:     global_buffer
      - .actual_access:  write_only
        .address_space:  global
        .offset:         16
        .size:           8
        .value_kind:     global_buffer
      - .actual_access:  read_only
        .address_space:  global
        .offset:         24
        .size:           8
        .value_kind:     global_buffer
      - .address_space:  global
        .offset:         32
        .size:           8
        .value_kind:     global_buffer
      - .actual_access:  read_only
        .address_space:  global
        .offset:         40
        .size:           8
        .value_kind:     global_buffer
      - .actual_access:  write_only
        .address_space:  global
        .offset:         48
        .size:           8
        .value_kind:     global_buffer
      - .address_space:  global
        .offset:         56
        .size:           8
        .value_kind:     global_buffer
    .group_segment_fixed_size: 0
    .kernarg_segment_align: 8
    .kernarg_segment_size: 64
    .language:       OpenCL C
    .language_version:
      - 2
      - 0
    .max_flat_workgroup_size: 512
    .name:           _Z7k_gemm1ILi1EEvPKDF16_S1_PDF16_PK15HIP_vector_typeIiLj2EEPKfS8_S2_PKt
    .private_segment_fixed_size: 0
    .sgpr_count:     100
    .sgpr_spill_count: 0
    .symbol:         _Z7k_gemm1ILi1EEvPKDF16_S1_PDF16_PK15HIP_vector_typeIiLj2EEPKfS8_S2_PKt.kd
    .uniform_work_group_size: 1
    .uses_dynamic_stack: false
    .vgpr_count:     254
    .vgpr_spill_count: 0
    .wavefront_size: 64
